# opt25: opt24 + acquire invalidate (buffer_inv sc1, L1-only) moved from barrier exit to barrier arrival, where it overlaps the arrival atomic; no cacheable loads are issued between arrival and completi
# baseline (speedup 1.0000x reference)
.LBB0_111:
	s_or_b64 exec, exec, s[4:5]
	v_readlane_b32 s4, v252, 22
	v_readlane_b32 s5, v252, 23
	s_waitcnt vmcnt(0)
	s_nop 2
	s_waitcnt vmcnt(0)

.LBB0_152:
	v_readlane_b32 s4, v252, 20
	v_readlane_b32 s5, v252, 21
	v_cvt_f32_u32_e32 v1, v2
	v_sub_u32_e32 v4, 0, v2
	v_rcp_iflag_f32_e32 v1, v1
	s_nop 1
	buffer_inv sc1
	global_atomic_add v3, v97, v197, s[4:5] sc0
	v_mul_f32_e32 v1, 0x4f7ffffe, v1
	v_cvt_u32_f32_e32 v1, v1
	v_mul_lo_u32 v4, v4, v1
	v_mul_hi_u32 v4, v1, v4
	v_add_u32_e32 v1, v1, v4
	s_waitcnt vmcnt(0)
	v_mul_hi_u32 v1, v3, v1
	v_mul_lo_u32 v4, v1, v2
	v_sub_u32_e32 v4, v3, v4
	v_add_u32_e32 v5, 1, v1
	v_cmp_ge_u32_e32 vcc, v4, v2
	v_add_u32_e32 v3, 1, v3
	s_nop 0
	v_cndmask_b32_e32 v1, v1, v5, vcc
	v_sub_u32_e32 v5, v4, v2
	v_cndmask_b32_e32 v4, v4, v5, vcc
	v_add_u32_e32 v5, 1, v1
	v_cmp_ge_u32_e32 vcc, v4, v2
	s_nop 1
	v_cndmask_b32_e32 v1, v1, v5, vcc
	v_mul_lo_u32 v4, v2, v1
	v_add_u32_e32 v2, v4, v2
	v_cmp_ne_u32_e32 vcc, v3, v2
	s_and_saveexec_b64 s[4:5], vcc
	s_xor_b64 s[4:5], exec, s[4:5]
	s_cbranch_execz .LBB0_166
	v_readlane_b32 s98, v251, 4
	v_add_u32_e32 v30, 1, v1
	v_mov_b32_e32 v31, s98
	ds_read_b32 v31, v31 offset:4
	s_waitcnt lgkmcnt(0)
	v_mul_lo_u32 v30, v30, v31
	v_readlane_b32 s6, v252, 24
	v_readlane_b32 s7, v252, 25
	s_waitcnt lgkmcnt(0)
	s_nop 3
	global_load_dword v0, v97, s[6:7] sc1
	s_waitcnt vmcnt(0)
	v_cmp_lt_u32_e32 vcc, v0, v30
	s_and_saveexec_b64 s[6:7], vcc
	s_cbranch_execz .LBB0_165
	s_mov_b32 s16, 1
	s_mov_b64 s[10:11], 0
	s_branch .LBB0_156

.LBB0_165:
	s_or_b64 exec, exec, s[6:7]
	s_waitcnt vmcnt(0)
	s_waitcnt vmcnt(0)

.LBB0_323:
	v_readlane_b32 s4, v252, 20
	v_readlane_b32 s5, v252, 21
	v_cvt_f32_u32_e32 v1, v2
	v_sub_u32_e32 v4, 0, v2
	v_rcp_iflag_f32_e32 v1, v1
	s_nop 1
	buffer_inv sc1
	global_atomic_add v3, v97, v197, s[4:5] sc0
	v_mul_f32_e32 v1, 0x4f7ffffe, v1
	v_cvt_u32_f32_e32 v1, v1
	v_mul_lo_u32 v4, v4, v1
	v_mul_hi_u32 v4, v1, v4
	v_add_u32_e32 v1, v1, v4
	s_waitcnt vmcnt(0)
	v_mul_hi_u32 v1, v3, v1
	v_mul_lo_u32 v4, v1, v2
	v_sub_u32_e32 v4, v3, v4
	v_add_u32_e32 v5, 1, v1
	v_cmp_ge_u32_e32 vcc, v4, v2
	v_add_u32_e32 v3, 1, v3
	s_nop 0
	v_cndmask_b32_e32 v1, v1, v5, vcc
	v_sub_u32_e32 v5, v4, v2
	v_cndmask_b32_e32 v4, v4, v5, vcc
	v_add_u32_e32 v5, 1, v1
	v_cmp_ge_u32_e32 vcc, v4, v2
	s_nop 1
	v_cndmask_b32_e32 v1, v1, v5, vcc
	v_mul_lo_u32 v4, v2, v1
	v_add_u32_e32 v2, v4, v2
	v_cmp_ne_u32_e32 vcc, v3, v2
	s_and_saveexec_b64 s[4:5], vcc
	s_xor_b64 s[4:5], exec, s[4:5]
	s_cbranch_execz .LBB0_337
	v_readlane_b32 s98, v251, 4
	v_add_u32_e32 v30, 1, v1
	v_mov_b32_e32 v31, s98
	ds_read_b32 v31, v31 offset:4
	s_waitcnt lgkmcnt(0)
	v_mul_lo_u32 v30, v30, v31
	v_readlane_b32 s6, v252, 24
	v_readlane_b32 s7, v252, 25
	s_waitcnt lgkmcnt(0)
	s_nop 3
	global_load_dword v0, v97, s[6:7] sc1
	s_waitcnt vmcnt(0)
	v_cmp_lt_u32_e32 vcc, v0, v30
	s_and_saveexec_b64 s[6:7], vcc
	s_cbranch_execz .LBB0_336
	s_mov_b32 s24, 1
	s_mov_b64 s[12:13], 0
	s_branch .LBB0_327

.LBB0_475:
	v_readlane_b32 s4, v252, 20
	v_readlane_b32 s5, v252, 21
	v_cvt_f32_u32_e32 v1, v2
	v_sub_u32_e32 v4, 0, v2
	v_rcp_iflag_f32_e32 v1, v1
	s_nop 1
	buffer_inv sc1
	global_atomic_add v3, v97, v197, s[4:5] sc0
	v_mul_f32_e32 v1, 0x4f7ffffe, v1
	v_cvt_u32_f32_e32 v1, v1
	v_mul_lo_u32 v4, v4, v1
	v_mul_hi_u32 v4, v1, v4
	v_add_u32_e32 v1, v1, v4
	s_waitcnt vmcnt(0)
	v_mul_hi_u32 v1, v3, v1
	v_mul_lo_u32 v4, v1, v2
	v_sub_u32_e32 v4, v3, v4
	v_add_u32_e32 v5, 1, v1
	v_cmp_ge_u32_e32 vcc, v4, v2
	v_add_u32_e32 v3, 1, v3
	s_nop 0
	v_cndmask_b32_e32 v1, v1, v5, vcc
	v_sub_u32_e32 v5, v4, v2
	v_cndmask_b32_e32 v4, v4, v5, vcc
	v_add_u32_e32 v5, 1, v1
	v_cmp_ge_u32_e32 vcc, v4, v2
	s_nop 1
	v_cndmask_b32_e32 v1, v1, v5, vcc
	v_mul_lo_u32 v4, v2, v1
	v_add_u32_e32 v2, v4, v2
	v_cmp_ne_u32_e32 vcc, v3, v2
	s_and_saveexec_b64 s[4:5], vcc
	s_xor_b64 s[4:5], exec, s[4:5]
	s_cbranch_execz .LBB0_489
	v_readlane_b32 s98, v251, 4
	v_add_u32_e32 v30, 1, v1
	v_mov_b32_e32 v31, s98
	ds_read_b32 v31, v31 offset:4
	s_waitcnt lgkmcnt(0)
	v_mul_lo_u32 v30, v30, v31
	v_readlane_b32 s6, v252, 24
	v_readlane_b32 s7, v252, 25
	s_waitcnt lgkmcnt(0)
	s_nop 3
	global_load_dword v0, v97, s[6:7] sc1
	s_waitcnt vmcnt(0)
	v_cmp_lt_u32_e32 vcc, v0, v30
	s_and_saveexec_b64 s[6:7], vcc
	s_cbranch_execz .LBB0_488
	s_mov_b32 s16, 1
	s_mov_b64 s[12:13], 0
	s_branch .LBB0_479

.LBB0_1193:
	v_readlane_b32 s4, v252, 20
	v_readlane_b32 s5, v252, 21
	v_cvt_f32_u32_e32 v1, v2
	v_sub_u32_e32 v4, 0, v2
	v_rcp_iflag_f32_e32 v1, v1
	s_nop 1
	buffer_inv sc1
	global_atomic_add v3, v97, v197, s[4:5] sc0
	v_mul_f32_e32 v1, 0x4f7ffffe, v1
	v_cvt_u32_f32_e32 v1, v1
	v_mul_lo_u32 v4, v4, v1
	v_mul_hi_u32 v4, v1, v4
	v_add_u32_e32 v1, v1, v4
	s_waitcnt vmcnt(0)
	v_mul_hi_u32 v1, v3, v1
	v_mul_lo_u32 v4, v1, v2
	v_sub_u32_e32 v4, v3, v4
	v_add_u32_e32 v5, 1, v1
	v_cmp_ge_u32_e32 vcc, v4, v2
	v_add_u32_e32 v3, 1, v3
	s_nop 0
	v_cndmask_b32_e32 v1, v1, v5, vcc
	v_sub_u32_e32 v5, v4, v2
	v_cndmask_b32_e32 v4, v4, v5, vcc
	v_add_u32_e32 v5, 1, v1
	v_cmp_ge_u32_e32 vcc, v4, v2
	s_nop 1
	v_cndmask_b32_e32 v1, v1, v5, vcc
	v_mul_lo_u32 v4, v2, v1
	v_add_u32_e32 v2, v4, v2
	v_cmp_ne_u32_e32 vcc, v3, v2
	s_and_saveexec_b64 s[4:5], vcc
	s_xor_b64 s[4:5], exec, s[4:5]
	s_cbranch_execz .LBB0_1207
	v_readlane_b32 s98, v251, 4
	v_add_u32_e32 v30, 1, v1
	v_mov_b32_e32 v31, s98
	ds_read_b32 v31, v31 offset:4
	s_waitcnt lgkmcnt(0)
	v_mul_lo_u32 v30, v30, v31
	v_readlane_b32 s6, v252, 24
	v_readlane_b32 s7, v252, 25
	s_waitcnt lgkmcnt(0)
	s_nop 3
	global_load_dword v0, v97, s[6:7] sc1
	s_waitcnt vmcnt(0)
	v_cmp_lt_u32_e32 vcc, v0, v30
	s_and_saveexec_b64 s[6:7], vcc
	s_cbranch_execz .LBB0_1206
	s_mov_b32 s20, 1
	s_mov_b64 s[8:9], 0
	s_branch .LBB0_1197

.LBB0_1479:
	v_readlane_b32 s4, v252, 20
	v_readlane_b32 s5, v252, 21
	v_cvt_f32_u32_e32 v1, v2
	v_sub_u32_e32 v4, 0, v2
	v_rcp_iflag_f32_e32 v1, v1
	s_nop 1
	buffer_inv sc1
	global_atomic_add v3, v97, v197, s[4:5] sc0
	v_mul_f32_e32 v1, 0x4f7ffffe, v1
	v_cvt_u32_f32_e32 v1, v1
	v_mul_lo_u32 v4, v4, v1
	v_mul_hi_u32 v4, v1, v4
	v_add_u32_e32 v1, v1, v4
	s_waitcnt vmcnt(0)
	v_mul_hi_u32 v1, v3, v1
	v_mul_lo_u32 v4, v1, v2
	v_sub_u32_e32 v4, v3, v4
	v_add_u32_e32 v5, 1, v1
	v_cmp_ge_u32_e32 vcc, v4, v2
	v_add_u32_e32 v3, 1, v3
	s_nop 0
	v_cndmask_b32_e32 v1, v1, v5, vcc
	v_sub_u32_e32 v5, v4, v2
	v_cndmask_b32_e32 v4, v4, v5, vcc
	v_add_u32_e32 v5, 1, v1
	v_cmp_ge_u32_e32 vcc, v4, v2
	s_nop 1
	v_cndmask_b32_e32 v1, v1, v5, vcc
	v_mul_lo_u32 v4, v2, v1
	v_add_u32_e32 v2, v4, v2
	v_cmp_ne_u32_e32 vcc, v3, v2
	s_and_saveexec_b64 s[4:5], vcc
	s_xor_b64 s[4:5], exec, s[4:5]
	s_cbranch_execz .LBB0_1493
	v_readlane_b32 s98, v251, 4
	v_add_u32_e32 v30, 1, v1
	v_mov_b32_e32 v31, s98
	ds_read_b32 v31, v31 offset:4
	s_waitcnt lgkmcnt(0)
	v_mul_lo_u32 v30, v30, v31
	v_readlane_b32 s6, v252, 24
	v_readlane_b32 s7, v252, 25
	s_waitcnt lgkmcnt(0)
	s_nop 3
	global_load_dword v0, v97, s[6:7] sc1
	s_waitcnt vmcnt(0)
	v_cmp_lt_u32_e32 vcc, v0, v30
	s_and_saveexec_b64 s[6:7], vcc
	s_cbranch_execz .LBB0_1492
	s_mov_b32 s16, 1
	s_mov_b64 s[8:9], 0
	s_branch .LBB0_1483
